# P7 w_out epilogue rewritten as a software-pipelined block (g1 hoisted, next sub-chunk loads in flight, counted vmcnt never covers a store) on top of KI tiling and gemv batching
# speedup vs baseline: 1.0148x; 1.0148x over previous
.LBB0_1643:
	s_ashr_i32 s21, s28, 5
	s_mul_i32 s30, s21, 0x1800
	v_lshl_add_u32 v152, s28, 8, v1
	s_ashr_i32 s31, s30, 31
	s_lshl_b32 s34, s21, 10
	s_lshl_b32 s28, s0, 2
	s_ashr_i32 s35, s34, 31
	s_ashr_i32 s29, s28, 31
	s_lshl_b64 s[30:31], s[30:31], 2
	v_lshl_or_b32 v148, s0, 8, v157
	s_add_u32 s0, s96, s30
	v_readlane_b32 s56, v254, 23
	s_addc_u32 s21, s97, s31
	v_ashrrev_i32_e32 v153, 31, v152
	v_readlane_b32 s57, v254, 24
	v_ashrrev_i32_e32 v149, 31, v148
	s_add_u32 s30, s0, 0x2000
	v_lshlrev_b64 v[146:147], 12, v[152:153]
	s_mov_b64 s[36:37], s[56:57]
	v_lshlrev_b64 v[178:179], 2, v[148:149]
	s_addc_u32 s31, s21, 0
	v_lshl_add_u64 v[146:147], s[36:37], 0, v[146:147]
	v_lshl_add_u64 v[154:155], s[30:31], 0, v[178:179]
	v_lshl_add_u64 v[180:181], v[146:147], 0, v[178:179]
	v_readlane_b32 s58, v254, 25
	v_readlane_b32 s59, v254, 26
	v_readlane_b32 s60, v254, 27
	v_readlane_b32 s61, v254, 28
	v_readlane_b32 s62, v254, 29
	v_readlane_b32 s63, v254, 30
	v_readlane_b32 s64, v254, 31
	v_readlane_b32 s65, v254, 32
	v_readlane_b32 s66, v254, 33
	v_readlane_b32 s67, v254, 34
	v_readlane_b32 s68, v254, 35
	v_readlane_b32 s69, v254, 36
	v_readlane_b32 s70, v254, 37
	v_readlane_b32 s71, v254, 38
	v_lshlrev_b64 v[182:183], 11, v[152:153]
	s_lshl_b64 s[34:35], s[34:35], 2
	v_lshlrev_b64 v[150:151], 1, v[148:149]
	v_lshl_add_u64 v[184:185], s[10:11], 0, v[182:183]
	s_add_u32 s34, s44, s34
	v_lshl_add_u64 v[184:185], v[184:185], 0, v[150:151]
	s_addc_u32 s35, s45, s35
	v_lshl_add_u64 v[146:147], s[34:35], 0, v[178:179]
	v_lshl_add_u64 v[182:183], s[12:13], 0, v[182:183]
	v_lshl_add_u64 v[182:183], v[182:183], 0, v[150:151]
	global_load_dwordx4 v[202:205], v[154:155], off
	global_load_dwordx4 v[206:209], v[154:155], off offset:16
	global_load_dwordx4 v[210:213], v[154:155], off offset:512
	global_load_dwordx4 v[214:217], v[154:155], off offset:528
	global_load_dwordx4 v[162:165], v[180:181], off
	global_load_dwordx4 v[166:169], v[180:181], off offset:16
	global_load_dwordx4 v[170:173], v[146:147], off
	global_load_dwordx4 v[174:177], v[146:147], off offset:16
	v_lshlrev_b64 v[148:149], 6, v[152:153]
	v_lshl_add_u64 v[148:149], s[14:15], 0, v[148:149]
	v_lshl_add_u64 v[148:149], s[28:29], 2, v[148:149]
	s_lshl_b32 s0, s46, 2
	v_add_co_u32_e32 v148, vcc, s0, v148
	s_nop 1
	v_addc_co_u32_e32 v149, vcc, 0, v149, vcc
	v_add_co_u32_e32 v152, vcc, 0x2000, v148
	s_nop 1
	v_addc_co_u32_e32 v153, vcc, 0, v149, vcc
	v_and_b32_e32 v151, 64, v161
	v_add_u32_e32 v151, 64, v151
	v_xor_b32_e32 v150, 16, v161
	v_cmp_lt_i32_e32 vcc, v150, v151
	s_nop 1
	v_cndmask_b32_e32 v150, v161, v150, vcc
	v_lshlrev_b32_e32 v178, 2, v150
	v_xor_b32_e32 v150, 32, v161
	v_cmp_lt_i32_e32 vcc, v150, v151
	s_nop 1
	v_cndmask_b32_e32 v150, v161, v150, vcc
	v_lshlrev_b32_e32 v179, 2, v150
	global_load_dwordx4 v[186:189], v[180:181], off offset:512
	global_load_dwordx4 v[190:193], v[180:181], off offset:528
	global_load_dwordx4 v[194:197], v[146:147], off offset:512
	global_load_dwordx4 v[218:221], v[146:147], off offset:528
	s_waitcnt vmcnt(4)
	v_pk_fma_f32 v[162:163], v[126:127], v[202:203], v[162:163]
	v_pk_fma_f32 v[164:165], v[128:129], v[204:205], v[164:165]
	v_pk_fma_f32 v[166:167], v[122:123], v[206:207], v[166:167]
	v_pk_fma_f32 v[168:169], v[124:125], v[208:209], v[168:169]
	v_cvt_pk_bf16_f32 v122, v162, v163
	v_cvt_pk_bf16_f32 v123, v164, v165
	v_cvt_pk_bf16_f32 v124, v166, v167
	v_cvt_pk_bf16_f32 v125, v168, v169
	global_store_dwordx4 v[184:185], v[122:125], off
	v_mul_f32_e32 v126, v163, v163
	v_fmac_f32_e32 v126, v162, v162
	v_mul_f32_e32 v127, v165, v165
	v_fmac_f32_e32 v127, v164, v164
	v_mul_f32_e32 v128, v167, v167
	v_fmac_f32_e32 v128, v166, v166
	v_mul_f32_e32 v129, v169, v169
	v_fmac_f32_e32 v129, v168, v168
	v_add_f32_e32 v126, v126, v127
	v_add_f32_e32 v126, v126, v128
	v_add_f32_e32 v126, v126, v129
	v_mov_b32_e32 v150, v126
	v_pk_mul_f32 v[170:171], v[162:163], v[170:171]
	v_pk_mul_f32 v[172:173], v[164:165], v[172:173]
	v_pk_mul_f32 v[174:175], v[166:167], v[174:175]
	v_pk_mul_f32 v[176:177], v[168:169], v[176:177]
	v_cvt_pk_bf16_f32 v126, v170, v171
	v_cvt_pk_bf16_f32 v127, v172, v173
	v_cvt_pk_bf16_f32 v128, v174, v175
	v_cvt_pk_bf16_f32 v129, v176, v177
	global_store_dwordx4 v[182:183], v[126:129], off
	v_add_co_u32_e32 v180, vcc, 0x10000, v180
	s_nop 1
	v_addc_co_u32_e32 v181, vcc, 0, v181, vcc
	global_load_dwordx4 v[162:165], v[180:181], off
	global_load_dwordx4 v[166:169], v[180:181], off offset:16
	global_load_dwordx4 v[170:173], v[146:147], off
	global_load_dwordx4 v[174:177], v[146:147], off offset:16
	s_waitcnt vmcnt(6)
	v_pk_fma_f32 v[186:187], v[118:119], v[210:211], v[186:187]
	v_pk_fma_f32 v[188:189], v[120:121], v[212:213], v[188:189]
	v_pk_fma_f32 v[190:191], v[114:115], v[214:215], v[190:191]
	v_pk_fma_f32 v[192:193], v[116:117], v[216:217], v[192:193]
	v_cvt_pk_bf16_f32 v114, v186, v187
	v_cvt_pk_bf16_f32 v115, v188, v189
	v_cvt_pk_bf16_f32 v116, v190, v191
	v_cvt_pk_bf16_f32 v117, v192, v193
	global_store_dwordx4 v[184:185], v[114:117], off offset:256
	v_mul_f32_e32 v118, v187, v187
	v_fmac_f32_e32 v118, v186, v186
	v_mul_f32_e32 v119, v189, v189
	v_fmac_f32_e32 v119, v188, v188
	v_mul_f32_e32 v120, v191, v191
	v_fmac_f32_e32 v120, v190, v190
	v_mul_f32_e32 v121, v193, v193
	v_fmac_f32_e32 v121, v192, v192
	v_add_f32_e32 v118, v118, v119
	v_add_f32_e32 v118, v118, v120
	v_add_f32_e32 v118, v118, v121
	v_add_f32_e32 v150, v150, v118
	v_pk_mul_f32 v[194:195], v[186:187], v[194:195]
	v_pk_mul_f32 v[196:197], v[188:189], v[196:197]
	v_pk_mul_f32 v[218:219], v[190:191], v[218:219]
	v_pk_mul_f32 v[220:221], v[192:193], v[220:221]
	v_cvt_pk_bf16_f32 v118, v194, v195
	v_cvt_pk_bf16_f32 v119, v196, v197
	v_cvt_pk_bf16_f32 v120, v218, v219
	v_cvt_pk_bf16_f32 v121, v220, v221
	global_store_dwordx4 v[182:183], v[118:121], off offset:256
	ds_bpermute_b32 v151, v178, v150
	s_waitcnt lgkmcnt(0)
	v_add_f32_e32 v150, v150, v151
	ds_bpermute_b32 v151, v179, v150
	s_waitcnt lgkmcnt(0)
	v_add_f32_e32 v150, v150, v151
	s_and_saveexec_b64 s[30:31], s[4:5]
	global_store_dword v[148:149], v150, off
	s_or_b64 exec, exec, s[30:31]
	v_add_co_u32_e32 v184, vcc, 0x8000, v184
	s_nop 1
	v_addc_co_u32_e32 v185, vcc, 0, v185, vcc
	v_add_co_u32_e32 v182, vcc, 0x8000, v182
	s_nop 1
	v_addc_co_u32_e32 v183, vcc, 0, v183, vcc
	global_load_dwordx4 v[186:189], v[180:181], off offset:512
	global_load_dwordx4 v[190:193], v[180:181], off offset:528
	global_load_dwordx4 v[194:197], v[146:147], off offset:512
	global_load_dwordx4 v[218:221], v[146:147], off offset:528
	s_waitcnt vmcnt(7)
	v_pk_fma_f32 v[162:163], v[110:111], v[202:203], v[162:163]
	v_pk_fma_f32 v[164:165], v[112:113], v[204:205], v[164:165]
	v_pk_fma_f32 v[166:167], v[106:107], v[206:207], v[166:167]
	v_pk_fma_f32 v[168:169], v[108:109], v[208:209], v[168:169]
	v_cvt_pk_bf16_f32 v106, v162, v163
	v_cvt_pk_bf16_f32 v107, v164, v165
	v_cvt_pk_bf16_f32 v108, v166, v167
	v_cvt_pk_bf16_f32 v109, v168, v169
	global_store_dwordx4 v[184:185], v[106:109], off
	v_mul_f32_e32 v110, v163, v163
	v_fmac_f32_e32 v110, v162, v162
	v_mul_f32_e32 v111, v165, v165
	v_fmac_f32_e32 v111, v164, v164
	v_mul_f32_e32 v112, v167, v167
	v_fmac_f32_e32 v112, v166, v166
	v_mul_f32_e32 v113, v169, v169
	v_fmac_f32_e32 v113, v168, v168
	v_add_f32_e32 v110, v110, v111
	v_add_f32_e32 v110, v110, v112
	v_add_f32_e32 v110, v110, v113
	v_mov_b32_e32 v150, v110
	v_pk_mul_f32 v[170:171], v[162:163], v[170:171]
	v_pk_mul_f32 v[172:173], v[164:165], v[172:173]
	v_pk_mul_f32 v[174:175], v[166:167], v[174:175]
	v_pk_mul_f32 v[176:177], v[168:169], v[176:177]
	v_cvt_pk_bf16_f32 v110, v170, v171
	v_cvt_pk_bf16_f32 v111, v172, v173
	v_cvt_pk_bf16_f32 v112, v174, v175
	v_cvt_pk_bf16_f32 v113, v176, v177
	global_store_dwordx4 v[182:183], v[110:113], off
	v_add_co_u32_e32 v180, vcc, 0x10000, v180
	s_nop 1
	v_addc_co_u32_e32 v181, vcc, 0, v181, vcc
	global_load_dwordx4 v[162:165], v[180:181], off
	global_load_dwordx4 v[166:169], v[180:181], off offset:16
	global_load_dwordx4 v[170:173], v[146:147], off
	global_load_dwordx4 v[174:177], v[146:147], off offset:16
	s_waitcnt vmcnt(6)
	v_pk_fma_f32 v[186:187], v[102:103], v[210:211], v[186:187]
	v_pk_fma_f32 v[188:189], v[104:105], v[212:213], v[188:189]
	v_pk_fma_f32 v[190:191], v[98:99], v[214:215], v[190:191]
	v_pk_fma_f32 v[192:193], v[100:101], v[216:217], v[192:193]
	v_cvt_pk_bf16_f32 v98, v186, v187
	v_cvt_pk_bf16_f32 v99, v188, v189
	v_cvt_pk_bf16_f32 v100, v190, v191
	v_cvt_pk_bf16_f32 v101, v192, v193
	global_store_dwordx4 v[184:185], v[98:101], off offset:256
	v_mul_f32_e32 v102, v187, v187
	v_fmac_f32_e32 v102, v186, v186
	v_mul_f32_e32 v103, v189, v189
	v_fmac_f32_e32 v103, v188, v188
	v_mul_f32_e32 v104, v191, v191
	v_fmac_f32_e32 v104, v190, v190
	v_mul_f32_e32 v105, v193, v193
	v_fmac_f32_e32 v105, v192, v192
	v_add_f32_e32 v102, v102, v103
	v_add_f32_e32 v102, v102, v104
	v_add_f32_e32 v102, v102, v105
	v_add_f32_e32 v150, v150, v102
	v_pk_mul_f32 v[194:195], v[186:187], v[194:195]
	v_pk_mul_f32 v[196:197], v[188:189], v[196:197]
	v_pk_mul_f32 v[218:219], v[190:191], v[218:219]
	v_pk_mul_f32 v[220:221], v[192:193], v[220:221]
	v_cvt_pk_bf16_f32 v102, v194, v195
	v_cvt_pk_bf16_f32 v103, v196, v197
	v_cvt_pk_bf16_f32 v104, v218, v219
	v_cvt_pk_bf16_f32 v105, v220, v221
	global_store_dwordx4 v[182:183], v[102:105], off offset:256
	ds_bpermute_b32 v151, v178, v150
	s_waitcnt lgkmcnt(0)
	v_add_f32_e32 v150, v150, v151
	ds_bpermute_b32 v151, v179, v150
	s_waitcnt lgkmcnt(0)
	v_add_f32_e32 v150, v150, v151
	s_and_saveexec_b64 s[30:31], s[4:5]
	global_store_dword v[148:149], v150, off offset:1024
	s_or_b64 exec, exec, s[30:31]
	v_add_co_u32_e32 v184, vcc, 0x8000, v184
	s_nop 1
	v_addc_co_u32_e32 v185, vcc, 0, v185, vcc
	v_add_co_u32_e32 v182, vcc, 0x8000, v182
	s_nop 1
	v_addc_co_u32_e32 v183, vcc, 0, v183, vcc
	global_load_dwordx4 v[186:189], v[180:181], off offset:512
	global_load_dwordx4 v[190:193], v[180:181], off offset:528
	global_load_dwordx4 v[194:197], v[146:147], off offset:512
	global_load_dwordx4 v[218:221], v[146:147], off offset:528
	s_waitcnt vmcnt(7)
	v_pk_fma_f32 v[162:163], v[94:95], v[202:203], v[162:163]
	v_pk_fma_f32 v[164:165], v[96:97], v[204:205], v[164:165]
	v_pk_fma_f32 v[166:167], v[90:91], v[206:207], v[166:167]
	v_pk_fma_f32 v[168:169], v[92:93], v[208:209], v[168:169]
	v_cvt_pk_bf16_f32 v90, v162, v163
	v_cvt_pk_bf16_f32 v91, v164, v165
	v_cvt_pk_bf16_f32 v92, v166, v167
	v_cvt_pk_bf16_f32 v93, v168, v169
	global_store_dwordx4 v[184:185], v[90:93], off
	v_mul_f32_e32 v94, v163, v163
	v_fmac_f32_e32 v94, v162, v162
	v_mul_f32_e32 v95, v165, v165
	v_fmac_f32_e32 v95, v164, v164
	v_mul_f32_e32 v96, v167, v167
	v_fmac_f32_e32 v96, v166, v166
	v_mul_f32_e32 v97, v169, v169
	v_fmac_f32_e32 v97, v168, v168
	v_add_f32_e32 v94, v94, v95
	v_add_f32_e32 v94, v94, v96
	v_add_f32_e32 v94, v94, v97
	v_mov_b32_e32 v150, v94
	v_pk_mul_f32 v[170:171], v[162:163], v[170:171]
	v_pk_mul_f32 v[172:173], v[164:165], v[172:173]
	v_pk_mul_f32 v[174:175], v[166:167], v[174:175]
	v_pk_mul_f32 v[176:177], v[168:169], v[176:177]
	v_cvt_pk_bf16_f32 v94, v170, v171
	v_cvt_pk_bf16_f32 v95, v172, v173
	v_cvt_pk_bf16_f32 v96, v174, v175
	v_cvt_pk_bf16_f32 v97, v176, v177
	global_store_dwordx4 v[182:183], v[94:97], off
	v_add_co_u32_e32 v180, vcc, 0x10000, v180
	s_nop 1
	v_addc_co_u32_e32 v181, vcc, 0, v181, vcc
	global_load_dwordx4 v[162:165], v[180:181], off
	global_load_dwordx4 v[166:169], v[180:181], off offset:16
	global_load_dwordx4 v[170:173], v[146:147], off
	global_load_dwordx4 v[174:177], v[146:147], off offset:16
	s_waitcnt vmcnt(6)
	v_pk_fma_f32 v[186:187], v[86:87], v[210:211], v[186:187]
	v_pk_fma_f32 v[188:189], v[88:89], v[212:213], v[188:189]
	v_pk_fma_f32 v[190:191], v[82:83], v[214:215], v[190:191]
	v_pk_fma_f32 v[192:193], v[84:85], v[216:217], v[192:193]
	v_cvt_pk_bf16_f32 v82, v186, v187
	v_cvt_pk_bf16_f32 v83, v188, v189
	v_cvt_pk_bf16_f32 v84, v190, v191
	v_cvt_pk_bf16_f32 v85, v192, v193
	global_store_dwordx4 v[184:185], v[82:85], off offset:256
	v_mul_f32_e32 v86, v187, v187
	v_fmac_f32_e32 v86, v186, v186
	v_mul_f32_e32 v87, v189, v189
	v_fmac_f32_e32 v87, v188, v188
	v_mul_f32_e32 v88, v191, v191
	v_fmac_f32_e32 v88, v190, v190
	v_mul_f32_e32 v89, v193, v193
	v_fmac_f32_e32 v89, v192, v192
	v_add_f32_e32 v86, v86, v87
	v_add_f32_e32 v86, v86, v88
	v_add_f32_e32 v86, v86, v89
	v_add_f32_e32 v150, v150, v86
	v_pk_mul_f32 v[194:195], v[186:187], v[194:195]
	v_pk_mul_f32 v[196:197], v[188:189], v[196:197]
	v_pk_mul_f32 v[218:219], v[190:191], v[218:219]
	v_pk_mul_f32 v[220:221], v[192:193], v[220:221]
	v_cvt_pk_bf16_f32 v86, v194, v195
	v_cvt_pk_bf16_f32 v87, v196, v197
	v_cvt_pk_bf16_f32 v88, v218, v219
	v_cvt_pk_bf16_f32 v89, v220, v221
	global_store_dwordx4 v[182:183], v[86:89], off offset:256
	ds_bpermute_b32 v151, v178, v150
	s_waitcnt lgkmcnt(0)
	v_add_f32_e32 v150, v150, v151
	ds_bpermute_b32 v151, v179, v150
	s_waitcnt lgkmcnt(0)
	v_add_f32_e32 v150, v150, v151
	s_and_saveexec_b64 s[30:31], s[4:5]
	global_store_dword v[148:149], v150, off offset:2048
	s_or_b64 exec, exec, s[30:31]
	v_add_co_u32_e32 v184, vcc, 0x8000, v184
	s_nop 1
	v_addc_co_u32_e32 v185, vcc, 0, v185, vcc
	v_add_co_u32_e32 v182, vcc, 0x8000, v182
	s_nop 1
	v_addc_co_u32_e32 v183, vcc, 0, v183, vcc
	global_load_dwordx4 v[186:189], v[180:181], off offset:512
	global_load_dwordx4 v[190:193], v[180:181], off offset:528
	global_load_dwordx4 v[194:197], v[146:147], off offset:512
	global_load_dwordx4 v[218:221], v[146:147], off offset:528
	s_waitcnt vmcnt(7)
	v_pk_fma_f32 v[162:163], v[78:79], v[202:203], v[162:163]
	v_pk_fma_f32 v[164:165], v[80:81], v[204:205], v[164:165]
	v_pk_fma_f32 v[166:167], v[74:75], v[206:207], v[166:167]
	v_pk_fma_f32 v[168:169], v[76:77], v[208:209], v[168:169]
	v_cvt_pk_bf16_f32 v74, v162, v163
	v_cvt_pk_bf16_f32 v75, v164, v165
	v_cvt_pk_bf16_f32 v76, v166, v167
	v_cvt_pk_bf16_f32 v77, v168, v169
	global_store_dwordx4 v[184:185], v[74:77], off
	v_mul_f32_e32 v78, v163, v163
	v_fmac_f32_e32 v78, v162, v162
	v_mul_f32_e32 v79, v165, v165
	v_fmac_f32_e32 v79, v164, v164
	v_mul_f32_e32 v80, v167, v167
	v_fmac_f32_e32 v80, v166, v166
	v_mul_f32_e32 v81, v169, v169
	v_fmac_f32_e32 v81, v168, v168
	v_add_f32_e32 v78, v78, v79
	v_add_f32_e32 v78, v78, v80
	v_add_f32_e32 v78, v78, v81
	v_mov_b32_e32 v150, v78
	v_pk_mul_f32 v[170:171], v[162:163], v[170:171]
	v_pk_mul_f32 v[172:173], v[164:165], v[172:173]
	v_pk_mul_f32 v[174:175], v[166:167], v[174:175]
	v_pk_mul_f32 v[176:177], v[168:169], v[176:177]
	v_cvt_pk_bf16_f32 v78, v170, v171
	v_cvt_pk_bf16_f32 v79, v172, v173
	v_cvt_pk_bf16_f32 v80, v174, v175
	v_cvt_pk_bf16_f32 v81, v176, v177
	global_store_dwordx4 v[182:183], v[78:81], off
	v_add_co_u32_e32 v180, vcc, 0x50000, v180
	s_nop 1
	v_addc_co_u32_e32 v181, vcc, 0, v181, vcc
	global_load_dwordx4 v[162:165], v[180:181], off
	global_load_dwordx4 v[166:169], v[180:181], off offset:16
	global_load_dwordx4 v[170:173], v[146:147], off
	global_load_dwordx4 v[174:177], v[146:147], off offset:16
	s_waitcnt vmcnt(6)
	v_pk_fma_f32 v[186:187], v[70:71], v[210:211], v[186:187]
	v_pk_fma_f32 v[188:189], v[72:73], v[212:213], v[188:189]
	v_pk_fma_f32 v[190:191], v[66:67], v[214:215], v[190:191]
	v_pk_fma_f32 v[192:193], v[68:69], v[216:217], v[192:193]
	v_cvt_pk_bf16_f32 v66, v186, v187
	v_cvt_pk_bf16_f32 v67, v188, v189
	v_cvt_pk_bf16_f32 v68, v190, v191
	v_cvt_pk_bf16_f32 v69, v192, v193
	global_store_dwordx4 v[184:185], v[66:69], off offset:256
	v_mul_f32_e32 v70, v187, v187
	v_fmac_f32_e32 v70, v186, v186
	v_mul_f32_e32 v71, v189, v189
	v_fmac_f32_e32 v71, v188, v188
	v_mul_f32_e32 v72, v191, v191
	v_fmac_f32_e32 v72, v190, v190
	v_mul_f32_e32 v73, v193, v193
	v_fmac_f32_e32 v73, v192, v192
	v_add_f32_e32 v70, v70, v71
	v_add_f32_e32 v70, v70, v72
	v_add_f32_e32 v70, v70, v73
	v_add_f32_e32 v150, v150, v70
	v_pk_mul_f32 v[194:195], v[186:187], v[194:195]
	v_pk_mul_f32 v[196:197], v[188:189], v[196:197]
	v_pk_mul_f32 v[218:219], v[190:191], v[218:219]
	v_pk_mul_f32 v[220:221], v[192:193], v[220:221]
	v_cvt_pk_bf16_f32 v70, v194, v195
	v_cvt_pk_bf16_f32 v71, v196, v197
	v_cvt_pk_bf16_f32 v72, v218, v219
	v_cvt_pk_bf16_f32 v73, v220, v221
	global_store_dwordx4 v[182:183], v[70:73], off offset:256
	ds_bpermute_b32 v151, v178, v150
	s_waitcnt lgkmcnt(0)
	v_add_f32_e32 v150, v150, v151
	ds_bpermute_b32 v151, v179, v150
	s_waitcnt lgkmcnt(0)
	v_add_f32_e32 v150, v150, v151
	s_and_saveexec_b64 s[30:31], s[4:5]
	global_store_dword v[148:149], v150, off offset:3072
	s_or_b64 exec, exec, s[30:31]
	v_add_co_u32_e32 v184, vcc, 0x28000, v184
	s_nop 1
	v_addc_co_u32_e32 v185, vcc, 0, v185, vcc
	v_add_co_u32_e32 v182, vcc, 0x28000, v182
	s_nop 1
	v_addc_co_u32_e32 v183, vcc, 0, v183, vcc
	global_load_dwordx4 v[186:189], v[180:181], off offset:512
	global_load_dwordx4 v[190:193], v[180:181], off offset:528
	global_load_dwordx4 v[194:197], v[146:147], off offset:512
	global_load_dwordx4 v[218:221], v[146:147], off offset:528
	s_waitcnt vmcnt(7)
	v_pk_fma_f32 v[162:163], v[62:63], v[202:203], v[162:163]
	v_pk_fma_f32 v[164:165], v[64:65], v[204:205], v[164:165]
	v_pk_fma_f32 v[166:167], v[58:59], v[206:207], v[166:167]
	v_pk_fma_f32 v[168:169], v[60:61], v[208:209], v[168:169]
	v_cvt_pk_bf16_f32 v58, v162, v163
	v_cvt_pk_bf16_f32 v59, v164, v165
	v_cvt_pk_bf16_f32 v60, v166, v167
	v_cvt_pk_bf16_f32 v61, v168, v169
	global_store_dwordx4 v[184:185], v[58:61], off
	v_mul_f32_e32 v62, v163, v163
	v_fmac_f32_e32 v62, v162, v162
	v_mul_f32_e32 v63, v165, v165
	v_fmac_f32_e32 v63, v164, v164
	v_mul_f32_e32 v64, v167, v167
	v_fmac_f32_e32 v64, v166, v166
	v_mul_f32_e32 v65, v169, v169
	v_fmac_f32_e32 v65, v168, v168
	v_add_f32_e32 v62, v62, v63
	v_add_f32_e32 v62, v62, v64
	v_add_f32_e32 v62, v62, v65
	v_mov_b32_e32 v150, v62
	v_pk_mul_f32 v[170:171], v[162:163], v[170:171]
	v_pk_mul_f32 v[172:173], v[164:165], v[172:173]
	v_pk_mul_f32 v[174:175], v[166:167], v[174:175]
	v_pk_mul_f32 v[176:177], v[168:169], v[176:177]
	v_cvt_pk_bf16_f32 v62, v170, v171
	v_cvt_pk_bf16_f32 v63, v172, v173
	v_cvt_pk_bf16_f32 v64, v174, v175
	v_cvt_pk_bf16_f32 v65, v176, v177
	global_store_dwordx4 v[182:183], v[62:65], off
	v_add_co_u32_e32 v180, vcc, 0x10000, v180
	s_nop 1
	v_addc_co_u32_e32 v181, vcc, 0, v181, vcc
	global_load_dwordx4 v[162:165], v[180:181], off
	global_load_dwordx4 v[166:169], v[180:181], off offset:16
	global_load_dwordx4 v[170:173], v[146:147], off
	global_load_dwordx4 v[174:177], v[146:147], off offset:16
	s_waitcnt vmcnt(6)
	v_pk_fma_f32 v[186:187], v[54:55], v[210:211], v[186:187]
	v_pk_fma_f32 v[188:189], v[56:57], v[212:213], v[188:189]
	v_pk_fma_f32 v[190:191], v[50:51], v[214:215], v[190:191]
	v_pk_fma_f32 v[192:193], v[52:53], v[216:217], v[192:193]
	v_cvt_pk_bf16_f32 v50, v186, v187
	v_cvt_pk_bf16_f32 v51, v188, v189
	v_cvt_pk_bf16_f32 v52, v190, v191
	v_cvt_pk_bf16_f32 v53, v192, v193
	global_store_dwordx4 v[184:185], v[50:53], off offset:256
	v_mul_f32_e32 v54, v187, v187
	v_fmac_f32_e32 v54, v186, v186
	v_mul_f32_e32 v55, v189, v189
	v_fmac_f32_e32 v55, v188, v188
	v_mul_f32_e32 v56, v191, v191
	v_fmac_f32_e32 v56, v190, v190
	v_mul_f32_e32 v57, v193, v193
	v_fmac_f32_e32 v57, v192, v192
	v_add_f32_e32 v54, v54, v55
	v_add_f32_e32 v54, v54, v56
	v_add_f32_e32 v54, v54, v57
	v_add_f32_e32 v150, v150, v54
	v_pk_mul_f32 v[194:195], v[186:187], v[194:195]
	v_pk_mul_f32 v[196:197], v[188:189], v[196:197]
	v_pk_mul_f32 v[218:219], v[190:191], v[218:219]
	v_pk_mul_f32 v[220:221], v[192:193], v[220:221]
	v_cvt_pk_bf16_f32 v54, v194, v195
	v_cvt_pk_bf16_f32 v55, v196, v197
	v_cvt_pk_bf16_f32 v56, v218, v219
	v_cvt_pk_bf16_f32 v57, v220, v221
	global_store_dwordx4 v[182:183], v[54:57], off offset:256
	ds_bpermute_b32 v151, v178, v150
	s_waitcnt lgkmcnt(0)
	v_add_f32_e32 v150, v150, v151
	ds_bpermute_b32 v151, v179, v150
	s_waitcnt lgkmcnt(0)
	v_add_f32_e32 v150, v150, v151
	s_and_saveexec_b64 s[30:31], s[4:5]
	global_store_dword v[152:153], v150, off
	s_or_b64 exec, exec, s[30:31]
	v_add_co_u32_e32 v184, vcc, 0x8000, v184
	s_nop 1
	v_addc_co_u32_e32 v185, vcc, 0, v185, vcc
	v_add_co_u32_e32 v182, vcc, 0x8000, v182
	s_nop 1
	v_addc_co_u32_e32 v183, vcc, 0, v183, vcc
	global_load_dwordx4 v[186:189], v[180:181], off offset:512
	global_load_dwordx4 v[190:193], v[180:181], off offset:528
	global_load_dwordx4 v[194:197], v[146:147], off offset:512
	global_load_dwordx4 v[218:221], v[146:147], off offset:528
	s_waitcnt vmcnt(7)
	v_pk_fma_f32 v[162:163], v[46:47], v[202:203], v[162:163]
	v_pk_fma_f32 v[164:165], v[48:49], v[204:205], v[164:165]
	v_pk_fma_f32 v[166:167], v[42:43], v[206:207], v[166:167]
	v_pk_fma_f32 v[168:169], v[44:45], v[208:209], v[168:169]
	v_cvt_pk_bf16_f32 v42, v162, v163
	v_cvt_pk_bf16_f32 v43, v164, v165
	v_cvt_pk_bf16_f32 v44, v166, v167
	v_cvt_pk_bf16_f32 v45, v168, v169
	global_store_dwordx4 v[184:185], v[42:45], off
	v_mul_f32_e32 v46, v163, v163
	v_fmac_f32_e32 v46, v162, v162
	v_mul_f32_e32 v47, v165, v165
	v_fmac_f32_e32 v47, v164, v164
	v_mul_f32_e32 v48, v167, v167
	v_fmac_f32_e32 v48, v166, v166
	v_mul_f32_e32 v49, v169, v169
	v_fmac_f32_e32 v49, v168, v168
	v_add_f32_e32 v46, v46, v47
	v_add_f32_e32 v46, v46, v48
	v_add_f32_e32 v46, v46, v49
	v_mov_b32_e32 v150, v46
	v_pk_mul_f32 v[170:171], v[162:163], v[170:171]
	v_pk_mul_f32 v[172:173], v[164:165], v[172:173]
	v_pk_mul_f32 v[174:175], v[166:167], v[174:175]
	v_pk_mul_f32 v[176:177], v[168:169], v[176:177]
	v_cvt_pk_bf16_f32 v46, v170, v171
	v_cvt_pk_bf16_f32 v47, v172, v173
	v_cvt_pk_bf16_f32 v48, v174, v175
	v_cvt_pk_bf16_f32 v49, v176, v177
	global_store_dwordx4 v[182:183], v[46:49], off
	v_add_co_u32_e32 v180, vcc, 0x10000, v180
	s_nop 1
	v_addc_co_u32_e32 v181, vcc, 0, v181, vcc
	global_load_dwordx4 v[162:165], v[180:181], off
	global_load_dwordx4 v[166:169], v[180:181], off offset:16
	global_load_dwordx4 v[170:173], v[146:147], off
	global_load_dwordx4 v[174:177], v[146:147], off offset:16
	s_waitcnt vmcnt(6)
	v_pk_fma_f32 v[186:187], v[38:39], v[210:211], v[186:187]
	v_pk_fma_f32 v[188:189], v[40:41], v[212:213], v[188:189]
	v_pk_fma_f32 v[190:191], v[34:35], v[214:215], v[190:191]
	v_pk_fma_f32 v[192:193], v[36:37], v[216:217], v[192:193]
	v_cvt_pk_bf16_f32 v34, v186, v187
	v_cvt_pk_bf16_f32 v35, v188, v189
	v_cvt_pk_bf16_f32 v36, v190, v191
	v_cvt_pk_bf16_f32 v37, v192, v193
	global_store_dwordx4 v[184:185], v[34:37], off offset:256
	v_mul_f32_e32 v38, v187, v187
	v_fmac_f32_e32 v38, v186, v186
	v_mul_f32_e32 v39, v189, v189
	v_fmac_f32_e32 v39, v188, v188
	v_mul_f32_e32 v40, v191, v191
	v_fmac_f32_e32 v40, v190, v190
	v_mul_f32_e32 v41, v193, v193
	v_fmac_f32_e32 v41, v192, v192
	v_add_f32_e32 v38, v38, v39
	v_add_f32_e32 v38, v38, v40
	v_add_f32_e32 v38, v38, v41
	v_add_f32_e32 v150, v150, v38
	v_pk_mul_f32 v[194:195], v[186:187], v[194:195]
	v_pk_mul_f32 v[196:197], v[188:189], v[196:197]
	v_pk_mul_f32 v[218:219], v[190:191], v[218:219]
	v_pk_mul_f32 v[220:221], v[192:193], v[220:221]
	v_cvt_pk_bf16_f32 v38, v194, v195
	v_cvt_pk_bf16_f32 v39, v196, v197
	v_cvt_pk_bf16_f32 v40, v218, v219
	v_cvt_pk_bf16_f32 v41, v220, v221
	global_store_dwordx4 v[182:183], v[38:41], off offset:256
	ds_bpermute_b32 v151, v178, v150
	s_waitcnt lgkmcnt(0)
	v_add_f32_e32 v150, v150, v151
	ds_bpermute_b32 v151, v179, v150
	s_waitcnt lgkmcnt(0)
	v_add_f32_e32 v150, v150, v151
	s_and_saveexec_b64 s[30:31], s[4:5]
	global_store_dword v[152:153], v150, off offset:1024
	s_or_b64 exec, exec, s[30:31]
	v_add_co_u32_e32 v184, vcc, 0x8000, v184
	s_nop 1
	v_addc_co_u32_e32 v185, vcc, 0, v185, vcc
	v_add_co_u32_e32 v182, vcc, 0x8000, v182
	s_nop 1
	v_addc_co_u32_e32 v183, vcc, 0, v183, vcc
	global_load_dwordx4 v[186:189], v[180:181], off offset:512
	global_load_dwordx4 v[190:193], v[180:181], off offset:528
	global_load_dwordx4 v[194:197], v[146:147], off offset:512
	global_load_dwordx4 v[218:221], v[146:147], off offset:528
	s_waitcnt vmcnt(7)
	v_pk_fma_f32 v[162:163], v[30:31], v[202:203], v[162:163]
	v_pk_fma_f32 v[164:165], v[32:33], v[204:205], v[164:165]
	v_pk_fma_f32 v[166:167], v[26:27], v[206:207], v[166:167]
	v_pk_fma_f32 v[168:169], v[28:29], v[208:209], v[168:169]
	v_cvt_pk_bf16_f32 v26, v162, v163
	v_cvt_pk_bf16_f32 v27, v164, v165
	v_cvt_pk_bf16_f32 v28, v166, v167
	v_cvt_pk_bf16_f32 v29, v168, v169
	global_store_dwordx4 v[184:185], v[26:29], off
	v_mul_f32_e32 v30, v163, v163
	v_fmac_f32_e32 v30, v162, v162
	v_mul_f32_e32 v31, v165, v165
	v_fmac_f32_e32 v31, v164, v164
	v_mul_f32_e32 v32, v167, v167
	v_fmac_f32_e32 v32, v166, v166
	v_mul_f32_e32 v33, v169, v169
	v_fmac_f32_e32 v33, v168, v168
	v_add_f32_e32 v30, v30, v31
	v_add_f32_e32 v30, v30, v32
	v_add_f32_e32 v30, v30, v33
	v_mov_b32_e32 v150, v30
	v_pk_mul_f32 v[170:171], v[162:163], v[170:171]
	v_pk_mul_f32 v[172:173], v[164:165], v[172:173]
	v_pk_mul_f32 v[174:175], v[166:167], v[174:175]
	v_pk_mul_f32 v[176:177], v[168:169], v[176:177]
	v_cvt_pk_bf16_f32 v30, v170, v171
	v_cvt_pk_bf16_f32 v31, v172, v173
	v_cvt_pk_bf16_f32 v32, v174, v175
	v_cvt_pk_bf16_f32 v33, v176, v177
	global_store_dwordx4 v[182:183], v[30:33], off
	v_add_co_u32_e32 v180, vcc, 0x10000, v180
	s_nop 1
	v_addc_co_u32_e32 v181, vcc, 0, v181, vcc
	global_load_dwordx4 v[162:165], v[180:181], off
	global_load_dwordx4 v[166:169], v[180:181], off offset:16
	global_load_dwordx4 v[170:173], v[146:147], off
	global_load_dwordx4 v[174:177], v[146:147], off offset:16
	s_waitcnt vmcnt(6)
	v_pk_fma_f32 v[186:187], v[22:23], v[210:211], v[186:187]
	v_pk_fma_f32 v[188:189], v[24:25], v[212:213], v[188:189]
	v_pk_fma_f32 v[190:191], v[18:19], v[214:215], v[190:191]
	v_pk_fma_f32 v[192:193], v[20:21], v[216:217], v[192:193]
	v_cvt_pk_bf16_f32 v18, v186, v187
	v_cvt_pk_bf16_f32 v19, v188, v189
	v_cvt_pk_bf16_f32 v20, v190, v191
	v_cvt_pk_bf16_f32 v21, v192, v193
	global_store_dwordx4 v[184:185], v[18:21], off offset:256
	v_mul_f32_e32 v22, v187, v187
	v_fmac_f32_e32 v22, v186, v186
	v_mul_f32_e32 v23, v189, v189
	v_fmac_f32_e32 v23, v188, v188
	v_mul_f32_e32 v24, v191, v191
	v_fmac_f32_e32 v24, v190, v190
	v_mul_f32_e32 v25, v193, v193
	v_fmac_f32_e32 v25, v192, v192
	v_add_f32_e32 v22, v22, v23
	v_add_f32_e32 v22, v22, v24
	v_add_f32_e32 v22, v22, v25
	v_add_f32_e32 v150, v150, v22
	v_pk_mul_f32 v[194:195], v[186:187], v[194:195]
	v_pk_mul_f32 v[196:197], v[188:189], v[196:197]
	v_pk_mul_f32 v[218:219], v[190:191], v[218:219]
	v_pk_mul_f32 v[220:221], v[192:193], v[220:221]
	v_cvt_pk_bf16_f32 v22, v194, v195
	v_cvt_pk_bf16_f32 v23, v196, v197
	v_cvt_pk_bf16_f32 v24, v218, v219
	v_cvt_pk_bf16_f32 v25, v220, v221
	global_store_dwordx4 v[182:183], v[22:25], off offset:256
	ds_bpermute_b32 v151, v178, v150
	s_waitcnt lgkmcnt(0)
	v_add_f32_e32 v150, v150, v151
	ds_bpermute_b32 v151, v179, v150
	s_waitcnt lgkmcnt(0)
	v_add_f32_e32 v150, v150, v151
	s_and_saveexec_b64 s[30:31], s[4:5]
	global_store_dword v[152:153], v150, off offset:2048
	s_or_b64 exec, exec, s[30:31]
	v_add_co_u32_e32 v184, vcc, 0x8000, v184
	s_nop 1
	v_addc_co_u32_e32 v185, vcc, 0, v185, vcc
	v_add_co_u32_e32 v182, vcc, 0x8000, v182
	s_nop 1
	v_addc_co_u32_e32 v183, vcc, 0, v183, vcc
	global_load_dwordx4 v[186:189], v[180:181], off offset:512
	global_load_dwordx4 v[190:193], v[180:181], off offset:528
	global_load_dwordx4 v[194:197], v[146:147], off offset:512
	global_load_dwordx4 v[218:221], v[146:147], off offset:528
	s_waitcnt vmcnt(7)
	v_pk_fma_f32 v[162:163], v[14:15], v[202:203], v[162:163]
	v_pk_fma_f32 v[164:165], v[16:17], v[204:205], v[164:165]
	v_pk_fma_f32 v[166:167], v[10:11], v[206:207], v[166:167]
	v_pk_fma_f32 v[168:169], v[12:13], v[208:209], v[168:169]
	v_cvt_pk_bf16_f32 v10, v162, v163
	v_cvt_pk_bf16_f32 v11, v164, v165
	v_cvt_pk_bf16_f32 v12, v166, v167
	v_cvt_pk_bf16_f32 v13, v168, v169
	global_store_dwordx4 v[184:185], v[10:13], off
	v_mul_f32_e32 v14, v163, v163
	v_fmac_f32_e32 v14, v162, v162
	v_mul_f32_e32 v15, v165, v165
	v_fmac_f32_e32 v15, v164, v164
	v_mul_f32_e32 v16, v167, v167
	v_fmac_f32_e32 v16, v166, v166
	v_mul_f32_e32 v17, v169, v169
	v_fmac_f32_e32 v17, v168, v168
	v_add_f32_e32 v14, v14, v15
	v_add_f32_e32 v14, v14, v16
	v_add_f32_e32 v14, v14, v17
	v_mov_b32_e32 v150, v14
	v_pk_mul_f32 v[170:171], v[162:163], v[170:171]
	v_pk_mul_f32 v[172:173], v[164:165], v[172:173]
	v_pk_mul_f32 v[174:175], v[166:167], v[174:175]
	v_pk_mul_f32 v[176:177], v[168:169], v[176:177]
	v_cvt_pk_bf16_f32 v14, v170, v171
	v_cvt_pk_bf16_f32 v15, v172, v173
	v_cvt_pk_bf16_f32 v16, v174, v175
	v_cvt_pk_bf16_f32 v17, v176, v177
	global_store_dwordx4 v[182:183], v[14:17], off
	s_waitcnt vmcnt(2)
	v_pk_fma_f32 v[186:187], v[6:7], v[210:211], v[186:187]
	v_pk_fma_f32 v[188:189], v[8:9], v[212:213], v[188:189]
	v_pk_fma_f32 v[190:191], v[2:3], v[214:215], v[190:191]
	v_pk_fma_f32 v[192:193], v[4:5], v[216:217], v[192:193]
	v_cvt_pk_bf16_f32 v2, v186, v187
	v_cvt_pk_bf16_f32 v3, v188, v189
	v_cvt_pk_bf16_f32 v4, v190, v191
	v_cvt_pk_bf16_f32 v5, v192, v193
	global_store_dwordx4 v[184:185], v[2:5], off offset:256
	v_mul_f32_e32 v6, v187, v187
	v_fmac_f32_e32 v6, v186, v186
	v_mul_f32_e32 v7, v189, v189
	v_fmac_f32_e32 v7, v188, v188
	v_mul_f32_e32 v8, v191, v191
	v_fmac_f32_e32 v8, v190, v190
	v_mul_f32_e32 v9, v193, v193
	v_fmac_f32_e32 v9, v192, v192
	v_add_f32_e32 v6, v6, v7
	v_add_f32_e32 v6, v6, v8
	v_add_f32_e32 v6, v6, v9
	v_add_f32_e32 v150, v150, v6
	v_pk_mul_f32 v[194:195], v[186:187], v[194:195]
	v_pk_mul_f32 v[196:197], v[188:189], v[196:197]
	v_pk_mul_f32 v[218:219], v[190:191], v[218:219]
	v_pk_mul_f32 v[220:221], v[192:193], v[220:221]
	v_cvt_pk_bf16_f32 v6, v194, v195
	v_cvt_pk_bf16_f32 v7, v196, v197
	v_cvt_pk_bf16_f32 v8, v218, v219
	v_cvt_pk_bf16_f32 v9, v220, v221
	global_store_dwordx4 v[182:183], v[6:9], off offset:256
	ds_bpermute_b32 v151, v178, v150
	s_waitcnt lgkmcnt(0)
	v_add_f32_e32 v150, v150, v151
	ds_bpermute_b32 v151, v179, v150
	s_waitcnt lgkmcnt(0)
	v_add_f32_e32 v150, v150, v151
	s_and_saveexec_b64 s[30:31], s[4:5]
	global_store_dword v[152:153], v150, off offset:3072
	s_or_b64 exec, exec, s[30:31]
	s_andn2_b64 vcc, exec, s[6:7]
	s_mov_b64 s[6:7], -1
	s_cbranch_vccnz .LBB0_1632
	s_andn2_b64 vcc, exec, s[8:9]
	s_cbranch_vccnz .LBB0_1631
	s_barrier
	s_branch .LBB0_1631
